# FIN loop: waits no longer drain the just-issued stores (row-1 loads waited with vmcnt(10) behind row 0's stores; loop-top WAW guard moved to the skipped-row edge)
# speedup vs baseline: 1.0006x; 1.0001x over previous
; template <int PH, bool PRB = false>
; __device__ __forceinline__ void run_phase(int layer, LAS unsigned char* lds, const int wv_) {
;     ...
;         for (int r0 = gw; r0 < S; r0 += 2 * NGW) {
;             u32x2 cc[2][4]; unsigned aa[2][4], bb[2][4];
; #pragma unroll
;             for (int q = 0; q < 2; ++q) { const int r = r0 + q * NGW < S ? r0 + q * NGW : r0;
;                 const u32x2* hr = (const u32x2*)(hb + (size_t)r * D); const unsigned* y0 = (const unsigned*)((const unsigned char*)ys + (size_t)(2 * r) * D); const unsigned* y1 = (const unsigned*)((const unsigned char*)ys + (size_t)(2 * r + 1) * D);
; #pragma unroll
;                 for (int j = 0; j < 4; ++j) { cc[q][j] = hr[lane + 64 * j]; aa[q][j] = y0[lane + 64 * j]; bb[q][j] = y1[lane + 64 * j]; } }
; #pragma unroll
;             for (int q = 0; q < 2; ++q) { const int r = r0 + q * NGW; if (r < S) {
;                 float4 v[4]; float ss = 0.f;
; #pragma unroll
;                 for (int j = 0; j < 4; ++j) {
;                     typedef float f2_ __attribute__((ext_vector_type(2)));
;                     const u32x2 c = cc[q][j]; const f2_ a0 = __builtin_amdgcn_cvt_pk_f32_fp8((int)aa[q][j], false), a1 = __builtin_amdgcn_cvt_pk_f32_fp8((int)aa[q][j], true), b0 = __builtin_amdgcn_cvt_pk_f32_fp8((int)bb[q][j], false), b1 = __builtin_amdgcn_cvt_pk_f32_fp8((int)bb[q][j], true);
;                     constexpr float iy = 1.0f / pg8::YS8_SCALE;
;                     v[j].x = __uint_as_float(c.x << 16) + (a0[0] + b0[0]) * iy; v[j].y = __uint_as_float(c.x & 0xffff0000u) + (a0[1] + b0[1]) * iy;
;                     v[j].z = __uint_as_float(c.y << 16) + (a1[0] + b1[0]) * iy; v[j].w = __uint_as_float(c.y & 0xffff0000u) + (a1[1] + b1[1]) * iy;
;                     ss += v[j].x * v[j].x + v[j].y * v[j].y + v[j].z * v[j].z + v[j].w * v[j].w;
;                 }
;                 ss = wave_sum(ss);
.LBB0_1762:
	s_add_i32 s3, s90, s2
	s_cmpk_lt_i32 s3, 0x4000
	s_cselect_b64 s[18:19], -1, 0
	v_lshl_add_u64 v[56:57], s[10:11], 0, v[20:21]
	s_and_b64 s[8:9], s[18:19], exec
	v_add_co_u32_e32 v32, vcc, s29, v56
	s_cselect_b32 s8, s3, s2
	s_ashr_i32 s13, s12, 31
	v_addc_co_u32_e32 v33, vcc, 0, v57, vcc
	s_lshl_b64 s[20:21], s[12:13], 10
	global_load_dwordx2 v[40:41], v[32:33], off
	global_load_dwordx2 v[42:43], v[32:33], off offset:1024
	global_load_dwordx2 v[50:51], v[32:33], off offset:1536
	global_load_dwordx2 v[44:45], v[32:33], off offset:512
	v_lshl_add_u64 v[32:33], v[18:19], 0, s[20:21]
	s_add_i32 s20, s12, 1
	s_ashr_i32 s21, s20, 31
	global_load_dword v92, v[32:33], off offset:768
	global_load_dword v52, v[32:33], off offset:256
	global_load_dword v72, v[32:33], off offset:512
	s_lshl_b64 s[20:21], s[20:21], 10
	global_load_dword v78, v[32:33], off
	v_lshl_add_u64 v[32:33], v[18:19], 0, s[20:21]
	global_load_dword v82, v[32:33], off
	global_load_dword v86, v[32:33], off offset:256
	global_load_dword v90, v[32:33], off offset:512
	global_load_dword v93, v[32:33], off offset:768
	s_lshl_b32 s20, s8, 1
	s_ashr_i32 s9, s8, 31
	s_ashr_i32 s21, s20, 31
	s_or_b32 s26, s20, 1
	s_lshl_b64 s[8:9], s[8:9], 11
	s_lshl_b64 s[20:21], s[20:21], 10
	s_ashr_i32 s27, s26, 31
	v_lshl_add_u64 v[32:33], v[16:17], 0, s[8:9]
	s_lshl_b64 s[8:9], s[26:27], 10
	v_lshl_add_u64 v[46:47], v[18:19], 0, s[20:21]
	global_load_dwordx2 v[38:39], v[32:33], off
	global_load_dwordx2 v[36:37], v[32:33], off offset:512
	global_load_dwordx2 v[34:35], v[32:33], off offset:1024
	s_nop 0
	global_load_dwordx2 v[32:33], v[32:33], off offset:1536
	v_lshl_add_u64 v[48:49], v[18:19], 0, s[8:9]
	global_load_dword v66, v[46:47], off
	global_load_dword v62, v[46:47], off offset:256
	global_load_dword v60, v[46:47], off offset:512
	global_load_dword v67, v[48:49], off
	global_load_dword v63, v[48:49], off offset:256
	global_load_dword v61, v[48:49], off offset:512
	global_load_dword v58, v[48:49], off offset:768
	global_load_dword v59, v[46:47], off offset:768
	s_mov_b64 s[20:21], -1
	s_and_b64 vcc, exec, s[0:1]
	s_waitcnt vmcnt(23)
	v_lshlrev_b32_e32 v46, 16, v40
	s_waitcnt vmcnt(22)
	v_lshlrev_b32_e32 v68, 16, v42
	v_and_b32_e32 v69, 0xffff0000, v42
	v_lshlrev_b32_e32 v70, 16, v43
	v_and_b32_e32 v71, 0xffff0000, v43
	v_and_b32_e32 v47, 0xffff0000, v40
	s_waitcnt vmcnt(18)
	v_cvt_pk_f32_fp8_e32 v[42:43], v52
	s_waitcnt vmcnt(17)
	v_cvt_pk_f32_fp8_e32 v[54:55], v72
	s_waitcnt vmcnt(15)
	v_cvt_pk_f32_fp8_e32 v[80:81], v82
	v_cvt_pk_f32_fp8_e32 v[76:77], v78
	s_waitcnt vmcnt(14)
	v_cvt_pk_f32_fp8_e32 v[84:85], v86
	v_cvt_pk_f32_fp8_sdwa v[78:79], v78 src0_sel:WORD_1
	v_cvt_pk_f32_fp8_sdwa v[82:83], v82 src0_sel:WORD_1
	s_waitcnt vmcnt(13)
	v_cvt_pk_f32_fp8_e32 v[88:89], v90
	v_cvt_pk_f32_fp8_sdwa v[52:53], v52 src0_sel:WORD_1
	v_cvt_pk_f32_fp8_sdwa v[72:73], v72 src0_sel:WORD_1
	v_cvt_pk_f32_fp8_sdwa v[86:87], v86 src0_sel:WORD_1
	v_cvt_pk_f32_fp8_sdwa v[90:91], v90 src0_sel:WORD_1
	v_lshlrev_b32_e32 v48, 16, v44
	v_and_b32_e32 v49, 0xffff0000, v44
	v_pk_add_f32 v[76:77], v[76:77], v[80:81]
	v_pk_add_f32 v[42:43], v[42:43], v[84:85]
	v_cvt_pk_f32_fp8_e32 v[74:75], v92
	v_pk_add_f32 v[78:79], v[78:79], v[82:83]
	v_pk_add_f32 v[82:83], v[54:55], v[88:89]
	v_pk_fma_f32 v[54:55], v[76:77], 0.5, v[46:47] op_sel_hi:[1,0,1]
	v_pk_fma_f32 v[46:47], v[42:43], 0.5, v[48:49] op_sel_hi:[1,0,1]
	s_waitcnt vmcnt(12)
	v_cvt_pk_f32_fp8_e32 v[48:49], v93
	v_lshlrev_b32_e32 v40, 16, v41
	v_and_b32_e32 v41, 0xffff0000, v41
	v_lshlrev_b32_e32 v44, 16, v45
	v_and_b32_e32 v45, 0xffff0000, v45
	v_pk_add_f32 v[80:81], v[52:53], v[86:87]
	v_pk_add_f32 v[72:73], v[72:73], v[90:91]
	v_pk_fma_f32 v[42:43], v[82:83], 0.5, v[68:69] op_sel_hi:[1,0,1]
	v_cvt_pk_f32_fp8_sdwa v[82:83], v92 src0_sel:WORD_1
	v_cvt_pk_f32_fp8_sdwa v[84:85], v93 src0_sel:WORD_1
	v_pk_fma_f32 v[52:53], v[78:79], 0.5, v[40:41] op_sel_hi:[1,0,1]
	v_pk_fma_f32 v[44:45], v[80:81], 0.5, v[44:45] op_sel_hi:[1,0,1]
	v_pk_fma_f32 v[40:41], v[72:73], 0.5, v[70:71] op_sel_hi:[1,0,1]
	v_pk_mul_f32 v[68:69], v[54:55], v[54:55]
	v_pk_mul_f32 v[72:73], v[46:47], v[46:47]
	v_pk_mul_f32 v[70:71], v[52:53], v[52:53]
	v_pk_mul_f32 v[76:77], v[44:45], v[44:45]
	v_pk_mul_f32 v[78:79], v[42:43], v[42:43]
	v_add_f32_e32 v72, v72, v73
	v_add_f32_e32 v68, v68, v69
	v_pk_mul_f32 v[80:81], v[40:41], v[40:41]
	v_lshlrev_b32_e32 v86, 16, v50
	v_and_b32_e32 v87, 0xffff0000, v50
	v_pk_add_f32 v[48:49], v[74:75], v[48:49]
	v_add_f32_e32 v72, v72, v76
	v_add_f32_e32 v68, v68, v70
	v_add_f32_e32 v69, v78, v79
	v_pk_fma_f32 v[48:49], v[48:49], 0.5, v[86:87] op_sel_hi:[1,0,1]
	v_lshlrev_b32_e32 v50, 16, v51
	v_and_b32_e32 v51, 0xffff0000, v51
	v_pk_add_f32 v[74:75], v[82:83], v[84:85]
	v_add_f32_e32 v72, v77, v72
	v_add_f32_e32 v68, v71, v68
	v_add_f32_e32 v69, v69, v80
	v_pk_fma_f32 v[50:51], v[74:75], 0.5, v[50:51] op_sel_hi:[1,0,1]
	v_pk_mul_f32 v[74:75], v[48:49], v[48:49]
	v_add_f32_e32 v68, v68, v72
	v_add_f32_e32 v69, v81, v69
	v_pk_mul_f32 v[82:83], v[50:51], v[50:51]
	v_add_f32_e32 v68, v68, v69
	v_add_f32_e32 v69, v74, v75
	v_add_f32_e32 v69, v69, v82
	v_add_f32_e32 v69, v83, v69
	v_add_f32_e32 v68, v68, v69
	ds_swizzle_b32 v69, v68 offset:swizzle(SWAP,1)
	s_waitcnt lgkmcnt(0)
	v_add_f32_e32 v68, v68, v69
	ds_swizzle_b32 v69, v68 offset:swizzle(SWAP,2)
	s_waitcnt lgkmcnt(0)
	v_add_f32_e32 v68, v68, v69
	ds_swizzle_b32 v69, v68 offset:swizzle(SWAP,4)
	s_waitcnt lgkmcnt(0)
	v_add_f32_e32 v68, v68, v69
	ds_swizzle_b32 v69, v68 offset:swizzle(SWAP,8)
	s_waitcnt lgkmcnt(0)
	v_add_f32_e32 v68, v68, v69
	ds_swizzle_b32 v69, v68 offset:swizzle(SWAP,16)
	s_waitcnt lgkmcnt(0)
	v_add_f32_e32 v68, v68, v69
	v_mov_b32_e32 v69, v68
	s_nop 1
	v_permlane32_swap_b32_e32 v68, v69
	v_add_f32_e32 v70, v68, v69
	v_fmamk_f32 v68, v70, 0x3a800000, v218
	v_cmp_gt_f32_e64 s[8:9], s61, v68
	v_mul_f32_e32 v69, 0x4b800000, v68
	s_cbranch_vccz .LBB0_1769
; template <int PH, bool PRB = false>
; __device__ __forceinline__ void run_phase(int layer, LAS unsigned char* lds, const int wv_) {
;     ...
;                     rms_row_bf16(v, 1.0f, nullptr, hbo + (size_t)r * D, lane);
;                     if (!PRB) {
;                         const float rs8 = rsqrtf(ss * (1.0f / D) + 1e-6f); unsigned char* h8 = ws + WS_H + 32 * MiB + (size_t)r * D;
; #pragma unroll
;                         for (int j = 0; j < 4; ++j) { int w = __builtin_amdgcn_cvt_pk_fp8_f32(v[j].x * rs8, v[j].y * rs8, 0, false); w = __builtin_amdgcn_cvt_pk_fp8_f32(v[j].z * rs8, v[j].w * rs8, w, true); ((int*)h8)[lane + 64 * j] = w; }
;                     }
;                     if (lane < 16) sso[(size_t)r * 16 + lane] = lane == 0 ? ss : 0.f;
	s_mov_b64 s[20:21], 0x4100000
	v_lshl_add_u64 v[72:73], v[56:57], 0, s[20:21]
	s_mov_b64 s[20:21], 0x4100600
	v_lshl_add_u64 v[74:75], v[56:57], 0, s[20:21]
	s_mov_b64 s[20:21], 0x4100400
	v_lshl_add_u64 v[76:77], v[56:57], 0, s[20:21]
	s_mov_b64 s[20:21], 0x4100200
	v_lshl_add_u64 v[56:57], v[56:57], 0, s[20:21]
	v_cvt_pk_bf16_f32 v78, v54, v55
	v_cvt_pk_bf16_f32 v79, v52, v53
	global_store_dwordx2 v[72:73], v[78:79], off
	v_cvt_pk_bf16_f32 v72, v46, v47
	v_cvt_pk_bf16_f32 v73, v44, v45
	global_store_dwordx2 v[56:57], v[72:73], off
	v_cvt_pk_bf16_f32 v56, v42, v43
	v_cvt_pk_bf16_f32 v57, v40, v41
	global_store_dwordx2 v[76:77], v[56:57], off
	v_cvt_pk_bf16_f32 v56, v48, v49
	v_cvt_pk_bf16_f32 v57, v50, v51
	global_store_dwordx2 v[74:75], v[56:57], off
	v_cndmask_b32_e64 v56, v68, v69, s[8:9]
	v_rsq_f32_e32 v56, v56
	v_mov_b32_e32 v74, v65
	v_lshl_add_u64 v[72:73], s[10:11], 0, v[30:31]
	s_mov_b32 s3, 0x2100000
	v_mul_f32_e32 v57, 0x45800000, v56
	v_cndmask_b32_e64 v56, v56, v57, s[8:9]
	v_mul_f32_e32 v57, v54, v56
	v_mul_f32_e32 v71, v55, v56
	v_cvt_pk_fp8_f32 v74, v57, v71
	v_mul_f32_e32 v57, v52, v56
	v_mul_f32_e32 v71, v53, v56
	v_add_co_u32_e32 v72, vcc, s3, v72
	v_cvt_pk_fp8_f32 v74, v57, v71 op_sel:[0,0,1]
	s_nop 0
	v_addc_co_u32_e32 v73, vcc, 0, v73, vcc
	v_mul_f32_e32 v57, v46, v56
	global_store_dword v[72:73], v74, off
	v_mul_f32_e32 v71, v47, v56
	v_mov_b32_e32 v74, v65
	v_cvt_pk_fp8_f32 v74, v57, v71
	v_mul_f32_e32 v57, v44, v56
	v_mul_f32_e32 v71, v45, v56
	v_cvt_pk_fp8_f32 v74, v57, v71 op_sel:[0,0,1]
	v_mul_f32_e32 v57, v42, v56
	v_mul_f32_e32 v71, v43, v56
	global_store_dword v[72:73], v74, off offset:256
	v_mov_b32_e32 v74, v65
	v_cvt_pk_fp8_f32 v74, v57, v71
	v_mul_f32_e32 v57, v40, v56
	v_mul_f32_e32 v71, v41, v56
	v_cvt_pk_fp8_f32 v74, v57, v71 op_sel:[0,0,1]
	v_mul_f32_e32 v57, v48, v56
	v_mul_f32_e32 v71, v49, v56
	global_store_dword v[72:73], v74, off offset:512
	v_mov_b32_e32 v74, v65
	v_cvt_pk_fp8_f32 v74, v57, v71
	v_mul_f32_e32 v57, v50, v56
	v_mul_f32_e32 v71, v51, v56
	v_cvt_pk_fp8_f32 v74, v57, v71 op_sel:[0,0,1]
	global_store_dword v[72:73], v74, off offset:768
	s_and_saveexec_b64 s[8:9], s[4:5]
	s_cbranch_execz .LBB0_1765
	v_cndmask_b32_e64 v57, 0, v70, s[6:7]
	v_lshl_add_u64 v[70:71], s[10:11], 0, v[28:29]
	global_store_dword v[70:71], v57, off

; template <int PH, bool PRB = false>
; __device__ __forceinline__ void run_phase(int layer, LAS unsigned char* lds, const int wv_) {
;     ...
;                     if (lane < 16) sso[(size_t)r * 16 + lane] = lane == 0 ? ss : 0.f;
;                     if (lane == 0 && !PRB) ((float*)(ws + WS_MISC + MISC_RSROW))[r] = rsqrtf(ss * (1.0f / D) + 1e-6f);
.LBB0_1767:
	s_or_b64 exec, exec, s[8:9]
	s_waitcnt vmcnt(10)

; template <int PH, bool PRB = false>
; __device__ __forceinline__ void run_phase(int layer, LAS unsigned char* lds, const int wv_) {
;     ...
;                 if (layer == DEPTH - 1) {
;                     const float rs = rsqrtf(ss * (1.0f / D) + 1e-6f); float4* o4 = (float4*)(p.out + (size_t)r * D);
; #pragma unroll
;                     for (int j = 0; j < 4; ++j) { const float4 gg = gfin[j]; float4 o; o.x = v[j].x * rs * gg.x; o.y = v[j].y * rs * gg.y; o.z = v[j].z * rs * gg.z; o.w = v[j].w * rs * gg.w; o4[lane + 64 * j] = o; }
.LBB0_1769:
	s_waitcnt vmcnt(0)
	s_and_b64 vcc, exec, s[20:21]
	s_cbranch_vccz .LBB0_1768
	v_cmp_gt_f32_e32 vcc, s61, v68
	s_nop 1
	v_cndmask_b32_e32 v56, v68, v69, vcc
	v_rsq_f32_e32 v68, v56
	v_lshl_add_u64 v[56:57], s[16:17], 0, v[64:65]
	v_mul_f32_e32 v69, 0x45800000, v68
	v_cndmask_b32_e32 v68, v68, v69, vcc
	v_pk_mul_f32 v[54:55], v[54:55], v[68:69] op_sel_hi:[1,0]
	v_pk_mul_f32 v[70:71], v[52:53], v[68:69] op_sel_hi:[1,0]
	v_pk_mul_f32 v[52:53], v[4:5], v[54:55]
	v_pk_mul_f32 v[54:55], v[6:7], v[70:71]
	v_pk_mul_f32 v[44:45], v[44:45], v[68:69] op_sel_hi:[1,0]
	v_pk_mul_f32 v[42:43], v[42:43], v[68:69] op_sel_hi:[1,0]
	v_pk_mul_f32 v[40:41], v[40:41], v[68:69] op_sel_hi:[1,0]
	global_store_dwordx4 v[56:57], v[52:55], off
	v_pk_mul_f32 v[42:43], v[12:13], v[42:43]
	v_pk_mul_f32 v[46:47], v[46:47], v[68:69] op_sel_hi:[1,0]
	v_pk_mul_f32 v[54:55], v[2:3], v[44:45]
	v_pk_mul_f32 v[44:45], v[14:15], v[40:41]
	global_store_dwordx4 v[56:57], v[42:45], off offset:2048
	v_pk_mul_f32 v[40:41], v[48:49], v[68:69] op_sel_hi:[1,0]
	v_pk_mul_f32 v[52:53], v[0:1], v[46:47]
	v_pk_mul_f32 v[42:43], v[50:51], v[68:69] op_sel_hi:[1,0]
	v_pk_mul_f32 v[40:41], v[8:9], v[40:41]
	v_pk_mul_f32 v[42:43], v[10:11], v[42:43]
	global_store_dwordx4 v[56:57], v[52:55], off offset:1024
	global_store_dwordx4 v[56:57], v[40:43], off offset:3072
	s_andn2_b64 vcc, exec, s[18:19]
	s_cbranch_vccnz .Lfin_skip1
; template <int PH, bool PRB = false>
; __device__ __forceinline__ void run_phase(int layer, LAS unsigned char* lds, const int wv_) {
;     ...
;                 for (int j = 0; j < 4; ++j) {
;                     typedef float f2_ __attribute__((ext_vector_type(2)));
;                     const u32x2 c = cc[q][j]; const f2_ a0 = __builtin_amdgcn_cvt_pk_f32_fp8((int)aa[q][j], false), a1 = __builtin_amdgcn_cvt_pk_f32_fp8((int)aa[q][j], true), b0 = __builtin_amdgcn_cvt_pk_f32_fp8((int)bb[q][j], false), b1 = __builtin_amdgcn_cvt_pk_f32_fp8((int)bb[q][j], true);
;                     constexpr float iy = 1.0f / pg8::YS8_SCALE;
;                     v[j].x = __uint_as_float(c.x << 16) + (a0[0] + b0[0]) * iy; v[j].y = __uint_as_float(c.x & 0xffff0000u) + (a0[1] + b0[1]) * iy;
;                     v[j].z = __uint_as_float(c.y << 16) + (a1[0] + b1[0]) * iy; v[j].w = __uint_as_float(c.y & 0xffff0000u) + (a1[1] + b1[1]) * iy;
;                     ss += v[j].x * v[j].x + v[j].y * v[j].y + v[j].z * v[j].z + v[j].w * v[j].w;
;                 }
;                 ss = wave_sum(ss);
;                 if (layer == DEPTH - 1) {
;                     const float rs = rsqrtf(ss * (1.0f / D) + 1e-6f); float4* o4 = (float4*)(p.out + (size_t)r * D);
; #pragma unroll
;                     for (int j = 0; j < 4; ++j) { const float4 gg = gfin[j]; float4 o; o.x = v[j].x * rs * gg.x; o.y = v[j].y * rs * gg.y; o.z = v[j].z * rs * gg.z; o.w = v[j].w * rs * gg.w; o4[lane + 64 * j] = o; }
;                 } else {
;                     rms_row_bf16(v, 1.0f, nullptr, hbo + (size_t)r * D, lane);
;                     if (!PRB) {
;                         const float rs8 = rsqrtf(ss * (1.0f / D) + 1e-6f); unsigned char* h8 = ws + WS_H + 32 * MiB + (size_t)r * D;
; #pragma unroll
;                         for (int j = 0; j < 4; ++j) { int w = __builtin_amdgcn_cvt_pk_fp8_f32(v[j].x * rs8, v[j].y * rs8, 0, false); w = __builtin_amdgcn_cvt_pk_fp8_f32(v[j].z * rs8, v[j].w * rs8, w, true); ((int*)h8)[lane + 64 * j] = w; }
;                     }
;                     if (lane < 16) sso[(size_t)r * 16 + lane] = lane == 0 ? ss : 0.f;
.LBB0_1771:
	v_cvt_pk_f32_fp8_e32 v[40:41], v66
	v_cvt_pk_f32_fp8_sdwa v[42:43], v66 src0_sel:WORD_1
	v_cvt_pk_f32_fp8_e32 v[44:45], v67
	v_cvt_pk_f32_fp8_sdwa v[46:47], v67 src0_sel:WORD_1
	v_lshlrev_b32_e32 v48, 16, v38
	v_and_b32_e32 v49, 0xffff0000, v38
	v_pk_add_f32 v[40:41], v[40:41], v[44:45]
	v_lshlrev_b32_e32 v38, 16, v39
	v_and_b32_e32 v39, 0xffff0000, v39
	v_pk_add_f32 v[42:43], v[42:43], v[46:47]
	v_cvt_pk_f32_fp8_sdwa v[44:45], v62 src0_sel:WORD_1
	v_cvt_pk_f32_fp8_sdwa v[52:53], v63 src0_sel:WORD_1
	v_pk_fma_f32 v[38:39], v[42:43], 0.5, v[38:39] op_sel_hi:[1,0,1]
	v_cvt_pk_f32_fp8_e32 v[42:43], v62
	v_cvt_pk_f32_fp8_e32 v[46:47], v63
	v_lshlrev_b32_e32 v54, 16, v36
	v_and_b32_e32 v55, 0xffff0000, v36
	v_lshlrev_b32_e32 v36, 16, v37
	v_and_b32_e32 v37, 0xffff0000, v37
	v_pk_add_f32 v[44:45], v[44:45], v[52:53]
	v_pk_add_f32 v[42:43], v[42:43], v[46:47]
	v_pk_fma_f32 v[36:37], v[44:45], 0.5, v[36:37] op_sel_hi:[1,0,1]
	v_cvt_pk_f32_fp8_e32 v[44:45], v60
	v_cvt_pk_f32_fp8_sdwa v[46:47], v60 src0_sel:WORD_1
	v_cvt_pk_f32_fp8_e32 v[56:57], v61
	v_cvt_pk_f32_fp8_sdwa v[60:61], v61 src0_sel:WORD_1
	v_lshlrev_b32_e32 v62, 16, v34
	v_and_b32_e32 v63, 0xffff0000, v34
	v_lshlrev_b32_e32 v34, 16, v35
	v_and_b32_e32 v35, 0xffff0000, v35
	v_pk_add_f32 v[46:47], v[46:47], v[60:61]
	v_pk_add_f32 v[44:45], v[44:45], v[56:57]
	v_pk_fma_f32 v[34:35], v[46:47], 0.5, v[34:35] op_sel_hi:[1,0,1]
	v_cvt_pk_f32_fp8_e32 v[46:47], v59
	v_cvt_pk_f32_fp8_e32 v[66:67], v58
	v_pk_fma_f32 v[40:41], v[40:41], 0.5, v[48:49] op_sel_hi:[1,0,1]
	v_pk_fma_f32 v[42:43], v[42:43], 0.5, v[54:55] op_sel_hi:[1,0,1]
	v_pk_fma_f32 v[44:45], v[44:45], 0.5, v[62:63] op_sel_hi:[1,0,1]
	v_cvt_pk_f32_fp8_sdwa v[62:63], v59 src0_sel:WORD_1
	v_cvt_pk_f32_fp8_sdwa v[58:59], v58 src0_sel:WORD_1
	v_pk_mul_f32 v[48:49], v[40:41], v[40:41]
	v_pk_mul_f32 v[52:53], v[42:43], v[42:43]
	v_pk_mul_f32 v[50:51], v[38:39], v[38:39]
	v_pk_mul_f32 v[54:55], v[36:37], v[36:37]
	v_pk_mul_f32 v[56:57], v[44:45], v[44:45]
	v_add_f32_e32 v52, v52, v53
	v_add_f32_e32 v48, v48, v49
	v_pk_mul_f32 v[60:61], v[34:35], v[34:35]
	v_lshlrev_b32_e32 v68, 16, v32
	v_and_b32_e32 v69, 0xffff0000, v32
	v_pk_add_f32 v[46:47], v[46:47], v[66:67]
	v_add_f32_e32 v52, v52, v54
	v_add_f32_e32 v48, v48, v50
	v_add_f32_e32 v49, v56, v57
	v_pk_fma_f32 v[46:47], v[46:47], 0.5, v[68:69] op_sel_hi:[1,0,1]
	v_lshlrev_b32_e32 v32, 16, v33
	v_and_b32_e32 v33, 0xffff0000, v33
	v_pk_add_f32 v[58:59], v[62:63], v[58:59]
	v_add_f32_e32 v52, v55, v52
	v_add_f32_e32 v48, v51, v48
	v_add_f32_e32 v49, v49, v60
	v_pk_fma_f32 v[32:33], v[58:59], 0.5, v[32:33] op_sel_hi:[1,0,1]
	v_pk_mul_f32 v[58:59], v[46:47], v[46:47]
	v_add_f32_e32 v48, v48, v52
	v_add_f32_e32 v49, v61, v49
	v_pk_mul_f32 v[62:63], v[32:33], v[32:33]
	v_add_f32_e32 v48, v48, v49
	v_add_f32_e32 v49, v58, v59
	v_add_f32_e32 v49, v49, v62
	v_add_f32_e32 v49, v63, v49
	v_add_f32_e32 v48, v48, v49
	ds_swizzle_b32 v49, v48 offset:swizzle(SWAP,1)
	s_mov_b64 s[18:19], -1
	s_andn2_b64 vcc, exec, s[0:1]
	s_waitcnt lgkmcnt(0)
	v_add_f32_e32 v48, v48, v49
	ds_swizzle_b32 v49, v48 offset:swizzle(SWAP,2)
	s_waitcnt lgkmcnt(0)
	v_add_f32_e32 v48, v48, v49
	ds_swizzle_b32 v49, v48 offset:swizzle(SWAP,4)
	s_waitcnt lgkmcnt(0)
	v_add_f32_e32 v48, v48, v49
	ds_swizzle_b32 v49, v48 offset:swizzle(SWAP,8)
	s_waitcnt lgkmcnt(0)
	v_add_f32_e32 v48, v48, v49
	ds_swizzle_b32 v49, v48 offset:swizzle(SWAP,16)
	s_waitcnt lgkmcnt(0)
	v_add_f32_e32 v48, v48, v49
	v_mov_b32_e32 v49, v48
	s_nop 1
	v_permlane32_swap_b32_e32 v48, v49
	v_add_f32_e32 v50, v48, v49
	v_fmamk_f32 v48, v50, 0x3a800000, v218
	v_cmp_gt_f32_e64 s[8:9], s61, v48
	v_mul_f32_e32 v49, 0x4b800000, v48
	s_cbranch_vccnz .LBB0_1777
	v_lshl_add_u64 v[54:55], s[10:11], 0, v[26:27]
	v_add_co_u32_e32 v54, vcc, s29, v54
	v_cndmask_b32_e64 v51, v48, v49, s[8:9]
	v_cvt_pk_bf16_f32 v52, v40, v41
	s_nop 0
	v_addc_co_u32_e32 v55, vcc, 0, v55, vcc
	v_rsq_f32_e32 v51, v51
	v_cvt_pk_bf16_f32 v53, v38, v39
	global_store_dwordx2 v[54:55], v[52:53], off
	v_cvt_pk_bf16_f32 v52, v42, v43
	v_cvt_pk_bf16_f32 v53, v36, v37
	global_store_dwordx2 v[54:55], v[52:53], off offset:512
	v_cvt_pk_bf16_f32 v52, v44, v45
	v_cvt_pk_bf16_f32 v53, v34, v35
	global_store_dwordx2 v[54:55], v[52:53], off offset:1024
	v_cvt_pk_bf16_f32 v52, v46, v47
	v_cvt_pk_bf16_f32 v53, v32, v33
	global_store_dwordx2 v[54:55], v[52:53], off offset:1536
	v_mul_f32_e32 v52, 0x45800000, v51
	v_cndmask_b32_e64 v51, v51, v52, s[8:9]
	v_mul_f32_e32 v52, v40, v51
	v_mul_f32_e32 v53, v41, v51
	v_mov_b32_e32 v54, v65
	v_cvt_pk_fp8_f32 v54, v52, v53
	v_mul_f32_e32 v52, v38, v51
	v_mul_f32_e32 v53, v39, v51
	s_mov_b32 s3, 0x2100000
	v_cvt_pk_fp8_f32 v54, v52, v53 op_sel:[0,0,1]
	v_lshl_add_u64 v[52:53], s[10:11], 0, v[24:25]
	v_add_co_u32_e32 v52, vcc, s3, v52
	v_mul_f32_e32 v55, v43, v51
	s_nop 0
	v_addc_co_u32_e32 v53, vcc, 0, v53, vcc
	global_store_dword v[52:53], v54, off
	v_mul_f32_e32 v54, v42, v51
	v_mov_b32_e32 v56, v65
	v_cvt_pk_fp8_f32 v56, v54, v55
	v_mul_f32_e32 v54, v36, v51
	v_mul_f32_e32 v55, v37, v51
	v_cvt_pk_fp8_f32 v56, v54, v55 op_sel:[0,0,1]
	v_mul_f32_e32 v54, v44, v51
	v_mul_f32_e32 v55, v45, v51
	global_store_dword v[52:53], v56, off offset:256
	v_mov_b32_e32 v56, v65
	v_cvt_pk_fp8_f32 v56, v54, v55
	v_mul_f32_e32 v54, v34, v51
	v_mul_f32_e32 v55, v35, v51
	v_cvt_pk_fp8_f32 v56, v54, v55 op_sel:[0,0,1]
	v_mul_f32_e32 v54, v46, v51
	v_mul_f32_e32 v55, v47, v51
	global_store_dword v[52:53], v56, off offset:512
	v_mov_b32_e32 v56, v65
	v_cvt_pk_fp8_f32 v56, v54, v55
	v_mul_f32_e32 v54, v32, v51
	v_mul_f32_e32 v55, v33, v51
	v_cvt_pk_fp8_f32 v56, v54, v55 op_sel:[0,0,1]
	global_store_dword v[52:53], v56, off offset:768
	s_and_saveexec_b64 s[8:9], s[4:5]
	s_cbranch_execz .LBB0_1774
	v_cndmask_b32_e64 v50, 0, v50, s[6:7]
	v_lshl_add_u64 v[52:53], s[10:11], 0, v[22:23]
	global_store_dword v[52:53], v50, off

; template <int PH, bool PRB = false>
; __device__ __forceinline__ void run_phase(int layer, LAS unsigned char* lds, const int wv_) {
;     ...
;         for (int r0 = gw; r0 < S; r0 += 2 * NGW) {
.Lfin_skip1:
	s_waitcnt vmcnt(0)
	s_branch .LBB0_1761
